# speedup vs baseline: 1.0073x; 1.0073x over previous
.LBB1_4:
	s_or_b64 exec, exec, s[2:3]
	s_mul_i32 s2, s22, 27
	s_mul_i32 s3, s26, 9
	s_and_b32 s27, s10, 63
	s_add_i32 s2, s2, s3
	s_mov_b32 s3, 0
	s_sub_i32 s13, s27, s12
	s_lshl_b64 s[10:11], s[2:3], 14
	s_waitcnt lgkmcnt(0)
	s_add_u32 s6, s6, s10
	s_addc_u32 s7, s7, s11
	s_max_i32 s31, s13, 0
	s_add_i32 s32, s27, s12
	s_min_u32 s32, s32, 63
	s_lshl_b32 s33, s22, 12
	s_lshl_b32 s34, s31, 6
	s_lshl_b32 s35, s27, 6
	s_lshl_b32 s36, s32, 6
	s_add_i32 s34, s34, s33
	s_add_i32 s35, s35, s33
	s_add_i32 s36, s36, s33
	v_and_b32_e32 v140, 31, v0
	v_lshrrev_b32_e32 v141, 2, v0
	v_and_or_b32 v142, v141, 32, v140
	v_subrev_u32_e32 v143, s12, v142
	v_add_u32_e32 v144, s12, v142
	v_max_i32_e32 v143, 0, v143
	v_min_u32_e32 v144, 63, v144
	v_add_lshl_u32 v145, v143, s34, 3
	global_load_dwordx2 v[122:123], v145, s[8:9]
	v_add_lshl_u32 v145, v142, s34, 3
	global_load_dwordx2 v[124:125], v145, s[8:9]
	v_add_lshl_u32 v145, v144, s34, 3
	global_load_dwordx2 v[126:127], v145, s[8:9]
	v_add_lshl_u32 v145, v143, s35, 3
	global_load_dwordx2 v[128:129], v145, s[8:9]
	v_add_lshl_u32 v145, v142, s35, 3
	global_load_dwordx2 v[130:131], v145, s[8:9]
	v_add_lshl_u32 v145, v144, s35, 3
	global_load_dwordx2 v[132:133], v145, s[8:9]
	v_add_lshl_u32 v145, v143, s36, 3
	global_load_dwordx2 v[134:135], v145, s[8:9]
	v_add_lshl_u32 v145, v142, s36, 3
	global_load_dwordx2 v[136:137], v145, s[8:9]
	v_add_lshl_u32 v145, v144, s36, 3
	global_load_dwordx2 v[138:139], v145, s[8:9]
	s_mov_b32 s23, s3
	s_max_i32 s2, s13, 0
	s_lshl_b64 s[10:11], s[22:23], 20
	s_lshl_b64 s[2:3], s[2:3], 14
	v_mov_b32_e32 v75, 0
	v_lshl_add_u64 v[76:77], v[74:75], 1, s[6:7]
	s_movk_i32 s6, 0x2000
	s_add_u32 s23, s4, s10
	v_lshrrev_b32_e32 v71, 4, v0
	v_add_co_u32_e32 v10, vcc, s6, v76
	s_addc_u32 s28, s5, s11
	v_add_u32_e32 v84, -3, v71
	v_addc_co_u32_e32 v11, vcc, 0, v77, vcc
	s_add_u32 s2, s23, s2
	v_max_i32_e32 v86, 0, v84
	global_load_dwordx4 v[6:9], v[10:11], off offset:-4096
	global_load_dwordx4 v[2:5], v[10:11], off
	s_addc_u32 s3, s28, s3
	v_lshlrev_b32_e32 v10, 8, v86
	v_mov_b32_e32 v11, v75
	v_and_b32_e32 v97, 0x78, v74
	v_lshl_add_u64 v[10:11], s[2:3], 0, v[10:11]
	v_lshlrev_b32_e32 v74, 1, v97
	v_lshl_add_u64 v[106:107], v[10:11], 0, v[74:75]
	v_or_b32_e32 v10, 0x100, v0
	v_lshrrev_b32_e32 v98, 4, v10
	v_add_u32_e32 v85, -3, v98
	v_and_b32_e32 v82, 0x78, v1
	v_or_b32_e32 v1, 0x200, v0
	v_lshlrev_b32_e32 v10, 8, v85
	v_mov_b32_e32 v11, v75
	v_lshrrev_b32_e32 v99, 4, v1
	s_movk_i32 s6, 0x4000
	v_lshl_add_u64 v[10:11], s[2:3], 0, v[10:11]
	v_lshlrev_b32_e32 v12, 1, v82
	v_mov_b32_e32 v13, v75
	v_add_u32_e32 v89, -3, v99
	v_or_b32_e32 v1, 0x300, v0
	v_add_co_u32_e32 v80, vcc, s6, v76
	v_lshl_add_u64 v[108:109], v[10:11], 0, v[12:13]
	v_lshlrev_b32_e32 v10, 8, v89
	v_mov_b32_e32 v11, v75
	v_lshrrev_b32_e32 v96, 4, v1
	v_addc_co_u32_e32 v81, vcc, 0, v77, vcc
	s_movk_i32 s6, 0x6000
	v_lshl_add_u64 v[10:11], s[2:3], 0, v[10:11]
	v_add_u32_e32 v90, -3, v96
	v_add_co_u32_e32 v94, vcc, s6, v76
	v_lshl_add_u64 v[110:111], v[10:11], 0, v[12:13]
	v_lshlrev_b32_e32 v10, 8, v90
	v_mov_b32_e32 v11, v75
	v_or_b32_e32 v93, 0x400, v0
	v_addc_co_u32_e32 v95, vcc, 0, v77, vcc
	s_mov_b32 s6, 0x8000
	v_lshl_add_u64 v[10:11], s[2:3], 0, v[10:11]
	v_min_u32_e32 v1, 0x45f, v93
	v_add_co_u32_e32 v100, vcc, s6, v76
	v_lshl_add_u64 v[112:113], v[10:11], 0, v[12:13]
	v_lshrrev_b32_e32 v10, 4, v1
	v_addc_co_u32_e32 v101, vcc, 0, v77, vcc
	s_mov_b32 s6, 0xa000
	v_add_u32_e32 v91, -3, v10
	v_add_co_u32_e32 v102, vcc, s6, v76
	v_min_u32_e32 v92, 63, v91
	v_lshlrev_b32_e32 v1, 3, v1
	v_addc_co_u32_e32 v103, vcc, 0, v77, vcc
	s_mov_b32 s6, 0xb000
	v_lshlrev_b32_e32 v10, 8, v92
	v_mov_b32_e32 v11, v75
	v_and_b32_e32 v1, 0x78, v1
	v_add_co_u32_e32 v104, vcc, s6, v76
	v_lshl_add_u64 v[10:11], s[2:3], 0, v[10:11]
	v_lshlrev_b32_e32 v78, 1, v1
	v_mov_b32_e32 v79, v75
	v_addc_co_u32_e32 v105, vcc, 0, v77, vcc
	v_lshl_add_u64 v[114:115], v[10:11], 0, v[78:79]
	global_load_dwordx4 v[58:61], v[80:81], off offset:-4096
	global_load_dwordx4 v[54:57], v[80:81], off
	global_load_dwordx4 v[50:53], v[94:95], off offset:-4096
	global_load_dwordx4 v[46:49], v[94:95], off
	global_load_dwordx4 v[38:41], v[100:101], off offset:-4096
	global_load_dwordx4 v[42:45], v[100:101], off
	global_load_dwordx4 v[30:33], v[102:103], off offset:-4096
	global_load_dwordx4 v[26:29], v[102:103], off
	global_load_dwordx4 v[66:69], v[106:107], off
	global_load_dwordx4 v[22:25], v[108:109], off
	global_load_dwordx4 v[18:21], v[110:111], off
	global_load_dwordx4 v[14:17], v[112:113], off
	global_load_dwordx4 v[10:13], v[114:115], off
	global_load_dwordx4 v[34:37], v[104:105], off
	global_load_dwordx4 v[62:65], v[76:77], off
	v_and_b32_e32 v95, 31, v0
	v_lshrrev_b32_e32 v1, 2, v0
	v_and_or_b32 v70, v1, 32, v95
	v_add_u32_e32 v79, s27, v72
	v_add_u32_e32 v94, v72, v70
	v_cmp_gt_u32_e64 s[6:7], 64, v79
	v_cmp_gt_u32_e64 s[2:3], 64, v94
	s_movk_i32 s10, 0x100
	s_and_b64 s[14:15], s[6:7], s[2:3]
	v_lshlrev_b32_e32 v1, 6, v79
	v_mov_b64_e32 v[72:73], 0
	v_add_u32_e32 v1, s12, v70
	v_cmp_gt_u32_e32 vcc, 64, v1
	v_add_u32_e32 v80, s26, v70
	s_add_i32 s29, s27, s12
	s_cmp_lt_u32 s29, 64
	s_cselect_b64 s[24:25], -1, 0
	v_max_i32_e32 v116, 0, v79
	v_max_i32_e32 v117, 0, v94
	v_min_u32_e32 v118, 63, v1
	s_min_u32 s10, s29, 63
	s_lshl_b32 s10, s10, 6
	s_lshl_b32 s11, s27, 6
	v_lshl_or_b32 v116, v116, 6, v83
	v_or_b32_e32 v119, s11, v83
	v_or_b32_e32 v120, s10, v83
	v_lshlrev_b32_e32 v75, 7, v86
	v_lshlrev_b32_e32 v88, 7, v85
	v_lshlrev_b32_e32 v87, 7, v89
	v_lshlrev_b32_e32 v86, 7, v90
	v_lshlrev_b32_e32 v79, 7, v92
	s_and_b64 s[14:15], s[6:7], s[2:3]
	s_and_b64 s[4:5], s[6:7], vcc
	s_and_b64 s[16:17], s[24:25], s[2:3]
	s_and_b64 s[18:19], s[24:25], vcc
	s_waitcnt vmcnt(17)
	v_cndmask_b32_e64 v122, 0, v122, s[14:15]
	v_cndmask_b32_e64 v123, 0, v123, s[14:15]
	v_add_f64 v[72:73], v[122:123], 0
	v_cndmask_b32_e64 v124, 0, v124, s[6:7]
	v_cndmask_b32_e64 v125, 0, v125, s[6:7]
	v_add_f64 v[72:73], v[72:73], v[124:125]
	v_cndmask_b32_e64 v126, 0, v126, s[4:5]
	v_cndmask_b32_e64 v127, 0, v127, s[4:5]
	v_add_f64 v[72:73], v[72:73], v[126:127]
	v_cndmask_b32_e64 v128, 0, v128, s[2:3]
	v_cndmask_b32_e64 v129, 0, v129, s[2:3]
	v_add_f64 v[72:73], v[72:73], v[128:129]
	v_add_f64 v[72:73], v[72:73], v[130:131]
	v_cndmask_b32_e64 v132, 0, v132, vcc
	v_cndmask_b32_e64 v133, 0, v133, vcc
	v_add_f64 v[72:73], v[72:73], v[132:133]
	v_cndmask_b32_e64 v134, 0, v134, s[16:17]
	v_cndmask_b32_e64 v135, 0, v135, s[16:17]
	v_add_f64 v[72:73], v[72:73], v[134:135]
	v_cndmask_b32_e64 v136, 0, v136, s[24:25]
	v_cndmask_b32_e64 v137, 0, v137, s[24:25]
	v_add_f64 v[72:73], v[72:73], v[136:137]
	v_cndmask_b32_e64 v138, 0, v138, s[18:19]
	v_cndmask_b32_e64 v139, 0, v139, s[18:19]
	v_add_f64 v[72:73], v[72:73], v[138:139]
	s_mov_b32 s32, 0
	s_brev_b32 s33, 8
	s_mov_b32 s34, 0x812dea11
	s_mov_b32 s35, 0x3d719799
	v_mov_b32_e32 v140, 0x100
	v_mov_b32_e32 v141, 0xffffff80
	v_mov_b32_e32 v142, 0x260
	v_cmp_gt_f64_e32 vcc, s[32:33], v[72:73]
	s_nop 1
	v_cndmask_b32_e32 v140, 0, v140, vcc
	v_ldexp_f64 v[144:145], v[72:73], v140
	v_rsq_f64_e32 v[146:147], v[144:145]
	v_cndmask_b32_e32 v141, 0, v141, vcc
	v_cmp_class_f64_e32 vcc, v[144:145], v142
	v_mul_f64 v[148:149], v[144:145], v[146:147]
	v_mul_f64 v[146:147], v[146:147], 0.5
	v_fma_f64 v[150:151], -v[146:147], v[148:149], 0.5
	v_fmac_f64_e32 v[148:149], v[148:149], v[150:151]
	v_fma_f64 v[152:153], -v[148:149], v[148:149], v[144:145]
	v_fmac_f64_e32 v[146:147], v[146:147], v[150:151]
	v_fmac_f64_e32 v[148:149], v[152:153], v[146:147]
	v_fma_f64 v[150:151], -v[148:149], v[148:149], v[144:145]
	v_fmac_f64_e32 v[148:149], v[150:151], v[146:147]
	v_ldexp_f64 v[146:147], v[148:149], v141
	v_cndmask_b32_e32 v145, v147, v145, vcc
	v_cndmask_b32_e32 v144, v146, v144, vcc
	v_max_f64 v[144:145], v[144:145], s[34:35]
	v_div_scale_f64 v[146:147], s[36:37], v[144:145], v[144:145], 1.0
	v_rcp_f64_e32 v[148:149], v[146:147]
	s_nop 1
	v_fma_f64 v[150:151], -v[146:147], v[148:149], 1.0
	v_fmac_f64_e32 v[148:149], v[148:149], v[150:151]
	v_fma_f64 v[150:151], -v[146:147], v[148:149], 1.0
	v_fmac_f64_e32 v[148:149], v[148:149], v[150:151]
	v_div_scale_f64 v[150:151], vcc, 1.0, v[144:145], 1.0
	v_mul_f64 v[152:153], v[150:151], v[148:149]
	v_fma_f64 v[146:147], -v[146:147], v[152:153], v[150:151]
	s_nop 1
	v_div_fmas_f64 v[146:147], v[146:147], v[148:149], v[152:153]
	v_div_fixup_f64 v[144:145], v[146:147], v[144:145], 1.0
	v_cvt_f32_f64_e32 v206, v[144:145]
	s_cmp_gt_i32 s13, -1
	s_cselect_b64 s[12:13], -1, 0
	v_cmp_gt_u32_e64 s[10:11], 64, v84
	v_cmp_gt_u32_e64 s[8:9], 64, v85
	v_cmp_gt_u32_e64 s[6:7], 64, v89
	v_cmp_gt_u32_e64 s[4:5], 64, v90
	v_cmp_gt_u32_e64 s[2:3], 64, v91
	s_and_b64 vcc, exec, s[12:13]
	v_lshrrev_b32_e32 v100, 4, v93
	s_cbranch_vccz .LBB1_29
	s_waitcnt vmcnt(6)
	v_cndmask_b32_e64 v102, 0, v66, s[10:11]
	v_mov_b32_e32 v66, 0x100
	v_lshl_add_u32 v66, v97, 1, v66
	s_movk_i32 s14, 0x110
	v_cndmask_b32_e64 v103, 0, v67, s[10:11]
	v_mad_u32_u24 v67, v71, s14, v66
	s_waitcnt vmcnt(0)
	ds_write_b128 v67, v[62:65] offset:19040
	v_mad_u32_u24 v62, v98, s14, v66
	ds_write_b128 v62, v[6:9] offset:19040
	v_mad_u32_u24 v6, v99, s14, v66
	ds_write_b128 v6, v[2:5] offset:19040
	v_mad_u32_u24 v2, v96, s14, v66
	ds_write_b128 v2, v[58:61] offset:19040
	v_mad_u32_u24 v2, v100, s14, v66
	ds_write_b128 v2, v[54:57] offset:19040
	v_or_b32_e32 v2, 0x500, v0
	v_lshrrev_b32_e32 v2, 4, v2
	v_mad_u32_u24 v2, v2, s14, v66
	ds_write_b128 v2, v[50:53] offset:19040
	v_or_b32_e32 v2, 0x600, v0
	v_lshrrev_b32_e32 v2, 4, v2
	v_mad_u32_u24 v2, v2, s14, v66
	ds_write_b128 v2, v[46:49] offset:19040
	v_or_b32_e32 v2, 0x700, v0
	v_lshrrev_b32_e32 v2, 4, v2
	v_mad_u32_u24 v2, v2, s14, v66
	ds_write_b128 v2, v[38:41] offset:19040
	ds_write_b128 v67, v[42:45] offset:53856
	v_or_b32_e32 v2, 0x900, v0
	v_lshrrev_b32_e32 v2, 4, v2
	v_mad_u32_u24 v2, v2, s14, v66
	ds_write_b128 v2, v[30:33] offset:19040
	v_or_b32_e32 v2, 0xa00, v0
	v_lshrrev_b32_e32 v2, 4, v2
	v_mad_u32_u24 v2, v2, s14, v66
	ds_write_b128 v2, v[26:29] offset:19040
	v_or_b32_e32 v2, 0xb00, v0
	v_lshrrev_b32_e32 v2, 4, v2
	v_mad_u32_u24 v2, v2, s14, v66
	s_movk_i32 s14, 0x360
	v_cmp_gt_u32_e32 vcc, s14, v0
	v_cndmask_b32_e64 v105, 0, v69, s[10:11]
	v_cndmask_b32_e64 v104, 0, v68, s[10:11]
	ds_write_b128 v2, v[34:37] offset:19040
	ds_write_b128 v67, v[102:105]
	s_and_saveexec_b64 s[14:15], vcc
	s_cbranch_execz .LBB1_22
	v_mul_u32_u24_e32 v6, 0x110, v98
	v_cndmask_b32_e64 v5, 0, v25, s[8:9]
	v_cndmask_b32_e64 v4, 0, v24, s[8:9]
	v_cndmask_b32_e64 v3, 0, v23, s[8:9]
	v_cndmask_b32_e64 v2, 0, v22, s[8:9]
	v_add_u32_e32 v6, v66, v6
	ds_write_b128 v6, v[2:5]

.LBB1_48:
	s_waitcnt vmcnt(0)
	s_lshl_b32 s4, s22, 6
	v_lshlrev_b32_e32 v16, 4, v92
	v_lshl_add_u32 v31, v17, 2, v16
	s_lshl_b32 s2, s26, 7
	s_add_i32 s2, s2, s4
	s_mov_b32 s3, 0
	v_or_b32_e32 v24, s2, v17
	v_mov_b32_e32 v25, 0
	v_mov_b32_e32 v30, v206
	s_nop 7
	s_nop 7
	v_lshlrev_b64 v[18:19], 14, v[24:25]
	v_lshl_add_u64 v[18:19], s[0:1], 0, v[18:19]
	s_lshl_b32 s2, s27, 8
	v_lshl_add_u64 v[20:21], v[18:19], 0, s[2:3]
	ds_read_b128 v[16:19], v31
	v_accvgpr_read_b32 v0, a0
	v_mov_b32_e32 v71, v25
	v_lshl_add_u64 v[26:27], v[70:71], 2, v[20:21]
	v_mul_f32_e32 v0, v0, v30
	v_lshlrev_b32_e32 v24, 16, v92
	v_accvgpr_read_b32 v1, a1
	ds_read_b128 v[20:23], v31 offset:32
	s_waitcnt lgkmcnt(1)
	v_mul_f32_e32 v0, v0, v16
	v_lshl_add_u64 v[28:29], v[26:27], 0, v[24:25]
	global_store_dword v[28:29], v0, off
	v_mul_f32_e32 v0, v1, v30
	v_mul_f32_e32 v16, v0, v17
	v_or_b32_e32 v0, 0x4000, v24
	v_mov_b32_e32 v1, v25
	v_accvgpr_read_b32 v2, a2
	v_lshl_add_u64 v[0:1], v[26:27], 0, v[0:1]
	global_store_dword v[0:1], v16, off
	v_mul_f32_e32 v0, v2, v30
	v_mul_f32_e32 v2, v0, v18
	v_or_b32_e32 v0, 0x8000, v24
	v_mov_b32_e32 v1, v25
	v_accvgpr_read_b32 v3, a3
	v_lshl_add_u64 v[0:1], v[26:27], 0, v[0:1]
	global_store_dword v[0:1], v2, off
	v_mul_f32_e32 v0, v3, v30
	v_mul_f32_e32 v2, v0, v19
	v_or_b32_e32 v0, 0xc000, v24
	v_mov_b32_e32 v1, v25
	v_accvgpr_read_b32 v4, a4
	v_lshl_add_u64 v[0:1], v[26:27], 0, v[0:1]
	global_store_dword v[0:1], v2, off
	v_mul_f32_e32 v0, v4, v30
	s_waitcnt lgkmcnt(0)
	v_mul_f32_e32 v2, v0, v20
	v_or_b32_e32 v0, 0x20000, v24
	v_mov_b32_e32 v1, v25
	v_accvgpr_read_b32 v5, a5
	v_lshl_add_u64 v[0:1], v[26:27], 0, v[0:1]
	global_store_dword v[0:1], v2, off
	v_mul_f32_e32 v0, v5, v30
	v_mul_f32_e32 v2, v0, v21
	v_or_b32_e32 v0, 0x24000, v24
	v_mov_b32_e32 v1, v25
	v_accvgpr_read_b32 v6, a6
	v_lshl_add_u64 v[0:1], v[26:27], 0, v[0:1]
	global_store_dword v[0:1], v2, off
	v_mul_f32_e32 v0, v6, v30
	v_mul_f32_e32 v2, v0, v22
	v_or_b32_e32 v0, 0x28000, v24
	v_mov_b32_e32 v1, v25
	v_accvgpr_read_b32 v7, a7
	v_lshl_add_u64 v[0:1], v[26:27], 0, v[0:1]
	global_store_dword v[0:1], v2, off
	v_mul_f32_e32 v0, v7, v30
	v_mul_f32_e32 v6, v0, v23
	ds_read_b128 v[0:3], v31 offset:64
	v_accvgpr_read_b32 v8, a8
	v_or_b32_e32 v4, 0x2c000, v24
	v_mov_b32_e32 v5, v25
	v_lshl_add_u64 v[4:5], v[26:27], 0, v[4:5]
	v_mul_f32_e32 v8, v8, v30
	v_or_b32_e32 v16, 0x40000, v24
	v_mov_b32_e32 v17, v25
	v_accvgpr_read_b32 v9, a9
	global_store_dword v[4:5], v6, off
	ds_read_b128 v[4:7], v31 offset:96
	s_waitcnt lgkmcnt(1)
	v_mul_f32_e32 v0, v8, v0
	v_lshl_add_u64 v[16:17], v[26:27], 0, v[16:17]
	global_store_dword v[16:17], v0, off
	v_mul_f32_e32 v0, v9, v30
	v_mul_f32_e32 v8, v0, v1
	v_or_b32_e32 v0, 0x44000, v24
	v_mov_b32_e32 v1, v25
	v_accvgpr_read_b32 v10, a10
	v_lshl_add_u64 v[0:1], v[26:27], 0, v[0:1]
	global_store_dword v[0:1], v8, off
	v_mul_f32_e32 v0, v10, v30
	v_mul_f32_e32 v2, v0, v2
	v_or_b32_e32 v0, 0x48000, v24
	v_mov_b32_e32 v1, v25
	v_accvgpr_read_b32 v11, a11
	v_lshl_add_u64 v[0:1], v[26:27], 0, v[0:1]
	global_store_dword v[0:1], v2, off
	v_mul_f32_e32 v0, v11, v30
	v_mul_f32_e32 v2, v0, v3
	v_or_b32_e32 v0, 0x4c000, v24
	v_mov_b32_e32 v1, v25
	v_accvgpr_read_b32 v12, a12
	v_lshl_add_u64 v[0:1], v[26:27], 0, v[0:1]
	global_store_dword v[0:1], v2, off
	v_mul_f32_e32 v0, v12, v30
	s_waitcnt lgkmcnt(0)
	v_mul_f32_e32 v2, v0, v4
	v_or_b32_e32 v0, 0x60000, v24
	v_mov_b32_e32 v1, v25
	v_accvgpr_read_b32 v13, a13
	v_lshl_add_u64 v[0:1], v[26:27], 0, v[0:1]
	global_store_dword v[0:1], v2, off
	v_mul_f32_e32 v0, v13, v30
	v_mul_f32_e32 v2, v0, v5
	v_or_b32_e32 v0, 0x64000, v24
	v_mov_b32_e32 v1, v25
	v_accvgpr_read_b32 v14, a14
	v_lshl_add_u64 v[0:1], v[26:27], 0, v[0:1]
	global_store_dword v[0:1], v2, off
	v_mul_f32_e32 v0, v14, v30
	v_mul_f32_e32 v2, v0, v6
	v_or_b32_e32 v0, 0x68000, v24
	v_mov_b32_e32 v1, v25
	v_accvgpr_read_b32 v15, a15
	v_lshl_add_u64 v[0:1], v[26:27], 0, v[0:1]
	global_store_dword v[0:1], v2, off
	v_mul_f32_e32 v0, v15, v30
	v_or_b32_e32 v24, 0x6c000, v24
	v_mul_f32_e32 v2, v0, v7
	v_lshl_add_u64 v[0:1], v[26:27], 0, v[24:25]
	global_store_dword v[0:1], v2, off
	s_endpgm

	.amdhsa_kernel _Z9k_coarse2PKtS0_PKdS2_Pf
		.amdhsa_group_segment_fixed_size 256
		.amdhsa_private_segment_fixed_size 0
		.amdhsa_kernarg_size 40
		.amdhsa_user_sgpr_count 2
		.amdhsa_user_sgpr_dispatch_ptr 0
		.amdhsa_user_sgpr_queue_ptr 0
		.amdhsa_user_sgpr_kernarg_segment_ptr 1
		.amdhsa_user_sgpr_dispatch_id 0
		.amdhsa_user_sgpr_kernarg_preload_length 0
		.amdhsa_user_sgpr_kernarg_preload_offset 0
		.amdhsa_user_sgpr_private_segment_size 0
		.amdhsa_uses_dynamic_stack 0
		.amdhsa_enable_private_segment 0
		.amdhsa_system_sgpr_workgroup_id_x 1
		.amdhsa_system_sgpr_workgroup_id_y 0
		.amdhsa_system_sgpr_workgroup_id_z 0
		.amdhsa_system_sgpr_workgroup_info 0
		.amdhsa_system_vgpr_workitem_id 0
		.amdhsa_next_free_vgpr 224
		.amdhsa_next_free_sgpr 38
		.amdhsa_accum_offset 208
		.amdhsa_reserve_vcc 1
		.amdhsa_float_round_mode_32 0
		.amdhsa_float_round_mode_16_64 0
		.amdhsa_float_denorm_mode_32 3
		.amdhsa_float_denorm_mode_16_64 3
		.amdhsa_dx10_clamp 1
		.amdhsa_ieee_mode 1
		.amdhsa_fp16_overflow 0
		.amdhsa_tg_split 0
		.amdhsa_exception_fp_ieee_invalid_op 0
		.amdhsa_exception_fp_denorm_src 0
		.amdhsa_exception_fp_ieee_div_zero 0
		.amdhsa_exception_fp_ieee_overflow 0
		.amdhsa_exception_fp_ieee_underflow 0
		.amdhsa_exception_fp_ieee_inexact 0
		.amdhsa_exception_int_div_zero 0
	.end_amdhsa_kernel

amdhsa.kernels:
  - .agpr_count:     0
    .args:
      - .actual_access:  read_only
        .address_space:  global
        .offset:         0
        .size:           8
        .value_kind:     global_buffer
      - .actual_access:  read_only
        .address_space:  global
        .offset:         8
        .size:           8
        .value_kind:     global_buffer
      - .actual_access:  write_only
        .address_space:  global
        .offset:         16
        .size:           8
        .value_kind:     global_buffer
      - .actual_access:  write_only
        .address_space:  global
        .offset:         24
        .size:           8
        .value_kind:     global_buffer
      - .actual_access:  write_only
        .address_space:  global
        .offset:         32
        .size:           8
        .value_kind:     global_buffer
      - .actual_access:  write_only
        .address_space:  global
        .offset:         40
        .size:           8
        .value_kind:     global_buffer
      - .actual_access:  write_only
        .address_space:  global
        .offset:         48
        .size:           8
        .value_kind:     global_buffer
      - .actual_access:  write_only
        .address_space:  global
        .offset:         56
        .size:           8
        .value_kind:     global_buffer
      - .actual_access:  write_only
        .address_space:  global
        .offset:         64
        .size:           8
        .value_kind:     global_buffer
    .group_segment_fixed_size: 18944
    .kernarg_segment_align: 8
    .kernarg_segment_size: 72
    .language:       OpenCL C
    .language_version:
      - 2
      - 0
    .max_flat_workgroup_size: 256
    .name:           _Z6k_prepPKfS0_PfS1_PdS2_PtS3_S3_
    .private_segment_fixed_size: 0
    .sgpr_count:     34
    .sgpr_spill_count: 0
    .symbol:         _Z6k_prepPKfS0_PfS1_PdS2_PtS3_S3_.kd
    .uniform_work_group_size: 1
    .uses_dynamic_stack: false
    .vgpr_count:     29
    .vgpr_spill_count: 0
    .wavefront_size: 64
  - .agpr_count:     16
    .args:
      - .actual_access:  read_only
        .address_space:  global
        .offset:         0
        .size:           8
        .value_kind:     global_buffer
      - .actual_access:  read_only
        .address_space:  global
        .offset:         8
        .size:           8
        .value_kind:     global_buffer
      - .actual_access:  read_only
        .address_space:  global
        .offset:         16
        .size:           8
        .value_kind:     global_buffer
      - .actual_access:  read_only
        .address_space:  global
        .offset:         24
        .size:           8
        .value_kind:     global_buffer
      - .actual_access:  write_only
        .address_space:  global
        .offset:         32
        .size:           8
        .value_kind:     global_buffer
    .group_segment_fixed_size: 256
    .kernarg_segment_align: 8
    .kernarg_segment_size: 40
    .language:       OpenCL C
    .language_version:
      - 2
      - 0
    .max_flat_workgroup_size: 256
    .name:           _Z9k_coarse2PKtS0_PKdS2_Pf
    .private_segment_fixed_size: 0
    .sgpr_count:     44
    .sgpr_spill_count: 0
    .symbol:         _Z9k_coarse2PKtS0_PKdS2_Pf.kd
    .uniform_work_group_size: 1
    .uses_dynamic_stack: false
    .vgpr_count:     224
    .vgpr_spill_count: 0
    .wavefront_size: 64
  - .agpr_count:     0
    .args:
      - .actual_access:  read_only
        .address_space:  global
        .offset:         0
        .size:           8
        .value_kind:     global_buffer
      - .actual_access:  read_only
        .address_space:  global
        .offset:         8
        .size:           8
        .value_kind:     global_buffer
      - .actual_access:  read_only
        .address_space:  global
        .offset:         16
        .size:           8
        .value_kind:     global_buffer
      - .actual_access:  read_only
        .address_space:  global
        .offset:         24
        .size:           8
        .value_kind:     global_buffer
      - .actual_access:  read_only
        .address_space:  global
        .offset:         32
        .size:           8
        .value_kind:     global_buffer
      - .actual_access:  read_only
        .address_space:  global
        .offset:         40
        .size:           8
        .value_kind:     global_buffer
      - .actual_access:  read_only
        .address_space:  global
        .offset:         48
        .size:           8
        .value_kind:     global_buffer
      - .actual_access:  write_only
        .address_space:  global
        .offset:         56
        .size:           8
        .value_kind:     global_buffer
      - .actual_access:  write_only
        .address_space:  global
        .offset:         64
        .size:           8
        .value_kind:     global_buffer
      - .actual_access:  write_only
        .address_space:  global
        .offset:         72
        .size:           8
        .value_kind:     global_buffer
      - .actual_access:  read_only
        .address_space:  global
        .offset:         80
        .size:           8
        .value_kind:     global_buffer
      - .actual_access:  read_only
        .address_space:  global
        .offset:         88
        .size:           8
        .value_kind:     global_buffer
      - .actual_access:  write_only
        .address_space:  global
        .offset:         96
        .size:           8
        .value_kind:     global_buffer
      - .actual_access:  write_only
        .address_space:  global
        .offset:         104
        .size:           8
        .value_kind:     global_buffer
    .group_segment_fixed_size: 30768
    .kernarg_segment_align: 8
    .kernarg_segment_size: 112
    .language:       OpenCL C
    .language_version:
      - 2
      - 0
    .max_flat_workgroup_size: 512
    .name:           _Z7k_fine3PKfS0_PKtS2_PKdS4_S0_PiPfS5_S0_S0_PtS7_
    .private_segment_fixed_size: 0
    .sgpr_count:     106
    .sgpr_spill_count: 4
    .symbol:         _Z7k_fine3PKfS0_PKtS2_PKdS4_S0_PiPfS5_S0_S0_PtS7_.kd
    .uniform_work_group_size: 1
    .uses_dynamic_stack: false
    .vgpr_count:     256
    .vgpr_spill_count: 0
    .wavefront_size: 64
  - .agpr_count:     0
    .args:
      - .actual_access:  read_only
        .address_space:  global
        .offset:         0
        .size:           8
        .value_kind:     global_buffer
      - .actual_access:  read_only
        .address_space:  global
        .offset:         8
        .size:           8
        .value_kind:     global_buffer
      - .actual_access:  read_only
        .address_space:  global
        .offset:         16
        .size:           8
        .value_kind:     global_buffer
      - .actual_access:  read_only
        .address_space:  global
        .offset:         24
        .size:           8
        .value_kind:     global_buffer
      - .actual_access:  read_only
        .address_space:  global
        .offset:         32
        .size:           8
        .value_kind:     global_buffer
      - .actual_access:  read_only
        .address_space:  global
        .offset:         40
        .size:           8
        .value_kind:     global_buffer
      - .actual_access:  write_only
        .address_space:  global
        .offset:         48
        .size:           8
        .value_kind:     global_buffer
      - .actual_access:  write_only
        .address_space:  global
        .offset:         56
        .size:           8
        .value_kind:     global_buffer
      - .actual_access:  write_only
        .address_space:  global
        .offset:         64
        .size:           8
        .value_kind:     global_buffer
    .group_segment_fixed_size: 18512
    .kernarg_segment_align: 8
    .kernarg_segment_size: 72
    .language:       OpenCL C
    .language_version:
      - 2
      - 0
    .max_flat_workgroup_size: 256
    .name:           _Z10k_transferPKtS0_PKfPKiS2_S4_PfS5_S5_
    .private_segment_fixed_size: 0
    .sgpr_count:     34
    .sgpr_spill_count: 0
    .symbol:         _Z10k_transferPKtS0_PKfPKiS2_S4_PfS5_S5_.kd
    .uniform_work_group_size: 1
    .uses_dynamic_stack: false
    .vgpr_count:     49
    .vgpr_spill_count: 0
    .wavefront_size: 64
